# expert-up + expert-down(main) padded-row MFMA skip; expert-down main epilogue left as the compiler scheduled it (1)
# speedup vs baseline: 1.0107x; 1.0034x over previous
; #define PG8_STAGE(bufoff, gbase, voff) do { _Pragma("unroll") for (int _i = 0; _i < 2; ++_i) \
;         __builtin_amdgcn_global_load_lds((const unsigned*)((const char*)(gbase) + (voff)[_i]), (LAS unsigned*)(lds + (bufoff) + ldsw + _i * 8192), 16, 0, 0); } while (0)
; #define PG8_LDA(dst, b, h) do { _Pragma("unroll") for (int m = 0; m < 4; ++m) dst[m] = PG8_LD8(lds + PG8_SA(b, h) + aoff + m * 2048); } while (0)
; #define PG8_LDB(dst, b, h) do { _Pragma("unroll") for (int n = 0; n < 2; ++n) dst[n] = PG8_LD8(lds + PG8_SB(b, h) + boff + n * 2048); } while (0)
; #define PG8_WAIT_V(n) asm volatile("s_waitcnt vmcnt(" #n ")" ::: "memory")
; #define PG8_WAIT_L(n) asm volatile("s_waitcnt lgkmcnt(" #n ")" ::: "memory")
; #define PG8_BAR __builtin_amdgcn_s_barrier()
; #define PG8_SCHED __builtin_amdgcn_sched_barrier(0)
;     ...
;         const bool has_next = S.next(ui + 1, nxt);
;         const char* nA = has_next ? nxt.A : cA; const char* nB = has_next ? nxt.B : cB;
;         for (int t = 0; t < nt; t += 2) {
;             const bool last = (t == nt - 2);
;             const char* a1 = cA + (size_t)(t + 1) * kstep;
;             const char* a2 = last ? nA : cA + (size_t)(t + 2) * kstep; const char* b2 = last ? nB : cB + (size_t)(t + 2) * kstep;
;             const char* a3 = a2 + kstep; const char* b3 = b2 + kstep;
;             if constexpr (SP2) {
;             PG8_LDB(B0, 0, 0); PG8_LDB(B1, 0, 1); PG8_SCHED; PG8_LDA(At, 0, 0); PG8_STAGE(PG8_SA(1, 1), a1 + hstep, voffA);
;             PG8_WAIT_V(8); PG8_WAIT_L(0); PG8_BAR; PG8_MMA(0, 0, At, B0); PG8_MMA(0, 1, At, B1); PG8_BAR; PG8_SCHED;
;             PG8_LDA(At, 0, 1); PG8_STAGE(PG8_SB(0, 0), b2, voffB); PG8_STAGE(PG8_SB(0, 1), b2 + hstep, voffB); PG8_STAGE(PG8_SA(0, 0), a2, voffA);
;             PG8_WAIT_V(8); PG8_WAIT_L(0); PG8_BAR; PG8_MMA(1, 0, At, B0); PG8_MMA(1, 1, At, B1); PG8_BAR; PG8_SCHED;
.LBB0_2335:
	ds_read_b128 v[18:21], v203
	ds_read_b128 v[22:25], v203 offset:1024
	ds_read_b128 v[26:29], v203 offset:2048
	ds_read_b128 v[30:33], v203 offset:3072
	ds_read_b128 v[2:5], v204
	ds_read_b128 v[6:9], v204 offset:1024
	ds_read_b128 v[10:13], v204 offset:2048
	ds_read_b128 v[14:17], v204 offset:3072
	s_add_i32 s81, s70, 2
	s_add_u32 s72, s68, 0x80
	s_addc_u32 s71, s69, 0
	s_cmp_eq_u32 s57, s70
	s_cselect_b32 s70, s62, s72
	s_cselect_b32 s71, s63, s71
	s_cselect_b32 s73, s65, s80
	s_cselect_b32 s72, s64, s61
	v_lshl_add_u64 v[184:185], s[68:69], 0, v[172:173]
	s_add_i32 m0, s21, 0xc000
	ds_read_b128 v[176:179], v205
	ds_read_b128 v[180:183], v205 offset:1024
	ds_read_b128 v[206:209], v205 offset:2048
	ds_read_b128 v[210:213], v205 offset:3072
	ds_read_b128 v[214:217], v205 offset:4096
	ds_read_b128 v[218:221], v205 offset:5120
	ds_read_b128 v[222:225], v205 offset:6144
	ds_read_b128 v[226:229], v205 offset:7168
	global_load_lds_dwordx4 v[184:185], off
	v_lshl_add_u64 v[184:185], s[68:69], 0, v[174:175]
	s_add_i32 m0, s21, 0xe000
	s_nop 0
	global_load_lds_dwordx4 v[184:185], off
	v_cmp_eq_f32_e32 vcc, 0, v252
	s_waitcnt vmcnt(8)
	s_waitcnt lgkmcnt(0)
	s_barrier
	s_cbranch_vccnz .Lp22sk_0
	s_setprio 1
	s_waitcnt lgkmcnt(0)
	v_mfma_f32_16x16x128_f8f6f4 v[158:161], v[18:25], v[176:183], v[158:161]
	v_mfma_f32_16x16x128_f8f6f4 v[154:157], v[26:33], v[176:183], v[154:157]
	v_mfma_f32_16x16x128_f8f6f4 v[142:145], v[18:25], v[206:213], v[142:145]
	v_mfma_f32_16x16x128_f8f6f4 v[138:141], v[26:33], v[206:213], v[138:141]
	v_mfma_f32_16x16x128_f8f6f4 v[126:129], v[18:25], v[214:221], v[126:129]
	v_mfma_f32_16x16x128_f8f6f4 v[122:125], v[26:33], v[214:221], v[122:125]
	v_mfma_f32_16x16x128_f8f6f4 v[110:113], v[18:25], v[222:229], v[110:113]
	v_mfma_f32_16x16x128_f8f6f4 v[106:109], v[26:33], v[222:229], v[106:109]
	s_nop 7
	s_setprio 0
	s_setprio 1
	v_mfma_f32_16x16x128_f8f6f4 v[150:153], v[2:9], v[176:183], v[150:153]
	v_mfma_f32_16x16x128_f8f6f4 v[146:149], v[10:17], v[176:183], v[146:149]
	v_mfma_f32_16x16x128_f8f6f4 v[134:137], v[2:9], v[206:213], v[134:137]
	v_mfma_f32_16x16x128_f8f6f4 v[130:133], v[10:17], v[206:213], v[130:133]
	v_mfma_f32_16x16x128_f8f6f4 v[118:121], v[2:9], v[214:221], v[118:121]
	v_mfma_f32_16x16x128_f8f6f4 v[114:117], v[10:17], v[214:221], v[114:117]
	v_mfma_f32_16x16x128_f8f6f4 v[102:105], v[2:9], v[222:229], v[102:105]
	v_mfma_f32_16x16x128_f8f6f4 v[98:101], v[10:17], v[222:229], v[98:101]
	s_nop 7
	s_setprio 0
.Lp22sk_0:
	s_barrier
	s_add_i32 s82, s59, s3
	v_lshl_add_u64 v[176:177], s[72:73], 0, v[164:165]
	s_mov_b32 m0, s82
	ds_read_b128 v[206:209], v205 offset:16384
	ds_read_b128 v[210:213], v205 offset:17408
	ds_read_b128 v[214:217], v205 offset:18432
	ds_read_b128 v[218:221], v205 offset:19456
	ds_read_b128 v[222:225], v205 offset:20480
	ds_read_b128 v[226:229], v205 offset:21504
	ds_read_b128 v[230:233], v205 offset:22528
	ds_read_b128 v[234:237], v205 offset:23552
	global_load_lds_dwordx4 v[176:177], off
	s_add_i32 m0, s82, 0x2000
	v_lshl_add_u64 v[178:179], s[72:73], 0, v[170:171]
	s_add_u32 s72, s72, s22
	s_addc_u32 s73, s73, s23
	s_add_i32 s82, s67, s3
	global_load_lds_dwordx4 v[178:179], off
	v_lshl_add_u64 v[180:181], s[72:73], 0, v[164:165]
	s_mov_b32 m0, s82
	v_lshl_add_u64 v[182:183], s[72:73], 0, v[170:171]
	global_load_lds_dwordx4 v[180:181], off
	s_add_i32 m0, s82, 0x2000
	v_lshl_add_u64 v[184:185], s[70:71], 0, v[166:167]
	global_load_lds_dwordx4 v[182:183], off
	s_mov_b32 m0, s21
	v_lshl_add_u64 v[186:187], s[70:71], 0, v[168:169]
	global_load_lds_dwordx4 v[184:185], off
	s_mov_b32 m0, s34
	s_nop 0
	global_load_lds_dwordx4 v[186:187], off
	v_cmp_eq_f32_e32 vcc, 0, v253
	s_waitcnt vmcnt(8)
	s_waitcnt lgkmcnt(0)
	s_barrier
	s_cbranch_vccnz .Lp22sk_1
	s_setprio 1
	s_waitcnt lgkmcnt(0)
	v_mfma_f32_16x16x128_f8f6f4 v[94:97], v[18:25], v[206:213], v[94:97]
	v_mfma_f32_16x16x128_f8f6f4 v[90:93], v[26:33], v[206:213], v[90:93]
	v_mfma_f32_16x16x128_f8f6f4 v[78:81], v[18:25], v[214:221], v[78:81]
	v_mfma_f32_16x16x128_f8f6f4 v[74:77], v[26:33], v[214:221], v[74:77]
	v_mfma_f32_16x16x128_f8f6f4 v[62:65], v[18:25], v[222:229], v[62:65]
	v_mfma_f32_16x16x128_f8f6f4 v[58:61], v[26:33], v[222:229], v[58:61]
	v_mfma_f32_16x16x128_f8f6f4 v[46:49], v[18:25], v[230:237], v[46:49]
	v_mfma_f32_16x16x128_f8f6f4 v[42:45], v[26:33], v[230:237], v[42:45]
	s_nop 7
	s_setprio 0
	s_setprio 1
	v_mfma_f32_16x16x128_f8f6f4 v[86:89], v[2:9], v[206:213], v[86:89]
	v_mfma_f32_16x16x128_f8f6f4 v[82:85], v[10:17], v[206:213], v[82:85]
	v_mfma_f32_16x16x128_f8f6f4 v[70:73], v[2:9], v[214:221], v[70:73]
	v_mfma_f32_16x16x128_f8f6f4 v[66:69], v[10:17], v[214:221], v[66:69]
	v_mfma_f32_16x16x128_f8f6f4 v[54:57], v[2:9], v[222:229], v[54:57]
	v_mfma_f32_16x16x128_f8f6f4 v[50:53], v[10:17], v[222:229], v[50:53]
	v_mfma_f32_16x16x128_f8f6f4 v[38:41], v[2:9], v[230:237], v[38:41]
	v_mfma_f32_16x16x128_f8f6f4 v[34:37], v[10:17], v[230:237], v[34:37]
	s_nop 7
	s_setprio 0
; #define PG8_STAGE(bufoff, gbase, voff) do { _Pragma("unroll") for (int _i = 0; _i < 2; ++_i) \
;         __builtin_amdgcn_global_load_lds((const unsigned*)((const char*)(gbase) + (voff)[_i]), (LAS unsigned*)(lds + (bufoff) + ldsw + _i * 8192), 16, 0, 0); } while (0)
; #define PG8_LDA(dst, b, h) do { _Pragma("unroll") for (int m = 0; m < 4; ++m) dst[m] = PG8_LD8(lds + PG8_SA(b, h) + aoff + m * 2048); } while (0)
; #define PG8_LDB(dst, b, h) do { _Pragma("unroll") for (int n = 0; n < 2; ++n) dst[n] = PG8_LD8(lds + PG8_SB(b, h) + boff + n * 2048); } while (0)
; #define PG8_WAIT_V(n) asm volatile("s_waitcnt vmcnt(" #n ")" ::: "memory")
; #define PG8_WAIT_L(n) asm volatile("s_waitcnt lgkmcnt(" #n ")" ::: "memory")
; #define PG8_BAR __builtin_amdgcn_s_barrier()
; #define PG8_SCHED __builtin_amdgcn_sched_barrier(0)
;     ...
;             PG8_LDB(B0, 1, 0); PG8_LDB(B1, 1, 1); PG8_SCHED; PG8_LDA(At, 1, 0); PG8_STAGE(PG8_SA(0, 1), a2 + hstep, voffA);
;             PG8_WAIT_V(8); PG8_WAIT_L(0); PG8_BAR; PG8_MMA(0, 0, At, B0); PG8_MMA(0, 1, At, B1); PG8_BAR; PG8_SCHED;
;             PG8_LDA(At, 1, 1); PG8_STAGE(PG8_SB(1, 0), b3, voffB); PG8_STAGE(PG8_SB(1, 1), b3 + hstep, voffB); PG8_STAGE(PG8_SA(1, 0), a3, voffA);
;             PG8_WAIT_V(8); PG8_WAIT_L(0); PG8_BAR; PG8_MMA(1, 0, At, B0); PG8_MMA(1, 1, At, B1); PG8_BAR; PG8_SCHED;
.Lp22sk_1:
	s_barrier
	s_add_i32 s72, 0, 0x18000
	s_add_i32 s73, 0, 0x1c000
	v_add_u32_e32 v14, s72, v201
	v_add_u32_e32 v30, s73, v201
	ds_read_b128 v[2:5], v14
	ds_read_b128 v[6:9], v14 offset:1024
	ds_read_b128 v[10:13], v14 offset:2048
	ds_read_b128 v[14:17], v14 offset:3072
	ds_read_b128 v[18:21], v30
	ds_read_b128 v[22:25], v30 offset:1024
	ds_read_b128 v[26:29], v30 offset:2048
	ds_read_b128 v[30:33], v30 offset:3072
	s_add_u32 s70, s70, s22
	s_addc_u32 s71, s71, s23
	s_mov_b32 m0, s35
	v_lshl_add_u64 v[238:239], s[70:71], 0, v[166:167]
	ds_read_b128 v[206:209], v205 offset:32768
	ds_read_b128 v[210:213], v205 offset:33792
	ds_read_b128 v[214:217], v205 offset:34816
	ds_read_b128 v[218:221], v205 offset:35840
	ds_read_b128 v[222:225], v205 offset:36864
	ds_read_b128 v[226:229], v205 offset:37888
	ds_read_b128 v[230:233], v205 offset:38912
	ds_read_b128 v[234:237], v205 offset:39936
	global_load_lds_dwordx4 v[238:239], off
	v_lshl_add_u64 v[238:239], s[70:71], 0, v[168:169]
	s_mov_b32 m0, s44
	s_nop 0
	global_load_lds_dwordx4 v[238:239], off
	v_cmp_eq_f32_e32 vcc, 0, v252
	s_waitcnt vmcnt(8)
	s_waitcnt lgkmcnt(0)
	s_barrier
	s_cbranch_vccnz .Lp22sk_2
	s_setprio 1
	s_waitcnt lgkmcnt(0)
	v_mfma_f32_16x16x128_f8f6f4 v[158:161], v[2:9], v[206:213], v[158:161]
	v_mfma_f32_16x16x128_f8f6f4 v[154:157], v[10:17], v[206:213], v[154:157]
	v_mfma_f32_16x16x128_f8f6f4 v[142:145], v[2:9], v[214:221], v[142:145]
	v_mfma_f32_16x16x128_f8f6f4 v[138:141], v[10:17], v[214:221], v[138:141]
	v_mfma_f32_16x16x128_f8f6f4 v[126:129], v[2:9], v[222:229], v[126:129]
	v_mfma_f32_16x16x128_f8f6f4 v[122:125], v[10:17], v[222:229], v[122:125]
	v_mfma_f32_16x16x128_f8f6f4 v[110:113], v[2:9], v[230:237], v[110:113]
	v_mfma_f32_16x16x128_f8f6f4 v[106:109], v[10:17], v[230:237], v[106:109]
	s_nop 7
	s_setprio 0
	s_setprio 1
	v_mfma_f32_16x16x128_f8f6f4 v[150:153], v[18:25], v[206:213], v[150:153]
	v_mfma_f32_16x16x128_f8f6f4 v[146:149], v[26:33], v[206:213], v[146:149]
	v_mfma_f32_16x16x128_f8f6f4 v[134:137], v[18:25], v[214:221], v[134:137]
	v_mfma_f32_16x16x128_f8f6f4 v[130:133], v[26:33], v[214:221], v[130:133]
	v_mfma_f32_16x16x128_f8f6f4 v[118:121], v[18:25], v[222:229], v[118:121]
	v_mfma_f32_16x16x128_f8f6f4 v[114:117], v[26:33], v[222:229], v[114:117]
	v_mfma_f32_16x16x128_f8f6f4 v[102:105], v[18:25], v[230:237], v[102:105]
	v_mfma_f32_16x16x128_f8f6f4 v[98:101], v[26:33], v[230:237], v[98:101]
	s_nop 7
	s_setprio 0
.Lp22sk_2:
	s_barrier
	s_add_i32 s70, s72, s3
	v_lshl_add_u64 v[176:177], v[176:177], 0, s[28:29]
	s_mov_b32 m0, s70
	ds_read_b128 v[206:209], v205 offset:49152
	ds_read_b128 v[210:213], v205 offset:50176
	ds_read_b128 v[214:217], v205 offset:51200
	ds_read_b128 v[218:221], v205 offset:52224
	ds_read_b128 v[222:225], v205 offset:53248
	ds_read_b128 v[226:229], v205 offset:54272
	ds_read_b128 v[230:233], v205 offset:55296
	ds_read_b128 v[234:237], v205 offset:56320
	global_load_lds_dwordx4 v[176:177], off
	v_lshl_add_u64 v[176:177], v[178:179], 0, s[28:29]
	s_add_i32 m0, s70, 0x2000
	s_add_i32 s70, s73, s3
	global_load_lds_dwordx4 v[176:177], off
	v_lshl_add_u64 v[176:177], v[180:181], 0, s[28:29]
	s_mov_b32 m0, s70
	s_nop 0
	global_load_lds_dwordx4 v[176:177], off
	v_lshl_add_u64 v[176:177], v[182:183], 0, s[28:29]
	s_add_i32 m0, s70, 0x2000
	s_nop 0
	global_load_lds_dwordx4 v[176:177], off
	v_lshl_add_u64 v[176:177], v[184:185], 0, s[28:29]
	s_mov_b32 m0, s50
	s_nop 0
	global_load_lds_dwordx4 v[176:177], off
	v_lshl_add_u64 v[176:177], v[186:187], 0, s[28:29]
	s_mov_b32 m0, s51
	s_nop 0
	global_load_lds_dwordx4 v[176:177], off
	v_cmp_eq_f32_e32 vcc, 0, v253
	s_waitcnt vmcnt(8)
	s_waitcnt lgkmcnt(0)
	s_barrier
	s_cbranch_vccnz .Lp22sk_3
	s_setprio 1
	s_waitcnt lgkmcnt(0)
	v_mfma_f32_16x16x128_f8f6f4 v[94:97], v[2:9], v[206:213], v[94:97]
	v_mfma_f32_16x16x128_f8f6f4 v[90:93], v[10:17], v[206:213], v[90:93]
	v_mfma_f32_16x16x128_f8f6f4 v[78:81], v[2:9], v[214:221], v[78:81]
	v_mfma_f32_16x16x128_f8f6f4 v[74:77], v[10:17], v[214:221], v[74:77]
	v_mfma_f32_16x16x128_f8f6f4 v[62:65], v[2:9], v[222:229], v[62:65]
	v_mfma_f32_16x16x128_f8f6f4 v[58:61], v[10:17], v[222:229], v[58:61]
	v_mfma_f32_16x16x128_f8f6f4 v[46:49], v[2:9], v[230:237], v[46:49]
	v_mfma_f32_16x16x128_f8f6f4 v[42:45], v[10:17], v[230:237], v[42:45]
	s_nop 7
	s_setprio 0
	s_setprio 1
	v_mfma_f32_16x16x128_f8f6f4 v[86:89], v[18:25], v[206:213], v[86:89]
	v_mfma_f32_16x16x128_f8f6f4 v[82:85], v[26:33], v[206:213], v[82:85]
	v_mfma_f32_16x16x128_f8f6f4 v[70:73], v[18:25], v[214:221], v[70:73]
	v_mfma_f32_16x16x128_f8f6f4 v[66:69], v[26:33], v[214:221], v[66:69]
	v_mfma_f32_16x16x128_f8f6f4 v[54:57], v[18:25], v[222:229], v[54:57]
	v_mfma_f32_16x16x128_f8f6f4 v[50:53], v[26:33], v[222:229], v[50:53]
	v_mfma_f32_16x16x128_f8f6f4 v[38:41], v[18:25], v[230:237], v[38:41]
	v_mfma_f32_16x16x128_f8f6f4 v[34:37], v[26:33], v[230:237], v[34:37]
	s_nop 7
	s_setprio 0
